# attention: wave 0 touches the next unit's first K/V tiles and Q rows (one dword per line) during the last key-loop trip, on top of v098
# baseline (speedup 1.0000x reference)
.LBB0_950:
	v_mov_b32_e32 v48, v173
	s_nop 1
	v_permlane32_swap_b32_e32 v173, v48
	v_add_f32_e32 v48, v173, v48
	v_div_scale_f32 v49, s[14:15], v48, v48, 1.0
	v_rcp_f32_e32 v50, v49
	s_lshl_b32 s64, s23, 7
	v_lshlrev_b32_e32 v208, 2, v188
	s_mov_b64 s[14:15], 0x23c00200
	v_fma_f32 v51, -v49, v50, 1.0
	v_fmac_f32_e32 v50, v51, v50
	v_div_scale_f32 v51, vcc, 1.0, v48, 1.0
	v_mul_f32_e32 v52, v51, v50
	v_fma_f32 v53, -v49, v52, v51
	v_fmac_f32_e32 v52, v53, v50
	v_fma_f32 v49, -v49, v52, v51
	v_div_fmas_f32 v49, v49, v50, v52
	v_lshlrev_b64 v[50:51], 11, v[200:201]
	v_lshl_add_u64 v[50:51], s[8:9], 0, v[50:51]
	v_lshl_add_u64 v[50:51], v[50:51], 0, s[64:65]
	v_div_fixup_f32 v48, v49, v48, 1.0
	v_lshl_add_u64 v[50:51], v[50:51], 0, v[208:209]
	v_lshl_add_u64 v[52:53], v[50:51], 0, s[14:15]
	v_pk_mul_f32 v[32:33], v[32:33], v[48:49] op_sel_hi:[1,0]
	v_pk_mul_f32 v[34:35], v[34:35], v[48:49] op_sel_hi:[1,0]
	v_pk_mul_f32 v[36:37], v[36:37], v[48:49] op_sel_hi:[1,0]
	v_pk_mul_f32 v[38:39], v[38:39], v[48:49] op_sel_hi:[1,0]
	v_cvt_pk_bf16_f32 v32, v32, v33
	v_cvt_pk_bf16_f32 v33, v34, v35
	v_cvt_pk_bf16_f32 v34, v36, v37
	v_cvt_pk_bf16_f32 v35, v38, v39
	v_pk_mul_f32 v[16:17], v[16:17], v[48:49] op_sel_hi:[1,0]
	v_pk_mul_f32 v[18:19], v[18:19], v[48:49] op_sel_hi:[1,0]
	v_pk_mul_f32 v[20:21], v[20:21], v[48:49] op_sel_hi:[1,0]
	v_pk_mul_f32 v[22:23], v[22:23], v[48:49] op_sel_hi:[1,0]
	v_cvt_pk_bf16_f32 v16, v16, v17
	v_cvt_pk_bf16_f32 v17, v18, v19
	v_cvt_pk_bf16_f32 v18, v20, v21
	v_cvt_pk_bf16_f32 v19, v22, v23
	v_permlane32_swap_b32_e32 v32, v34
	v_permlane32_swap_b32_e32 v33, v35
	global_store_dwordx4 v[52:53], v[32:35], off
	v_pk_mul_f32 v[40:41], v[40:41], v[48:49] op_sel_hi:[1,0]
	v_pk_mul_f32 v[42:43], v[42:43], v[48:49] op_sel_hi:[1,0]
	v_pk_mul_f32 v[44:45], v[44:45], v[48:49] op_sel_hi:[1,0]
	v_pk_mul_f32 v[46:47], v[46:47], v[48:49] op_sel_hi:[1,0]
	v_cvt_pk_bf16_f32 v40, v40, v41
	v_cvt_pk_bf16_f32 v41, v42, v43
	v_cvt_pk_bf16_f32 v42, v44, v45
	v_cvt_pk_bf16_f32 v43, v46, v47
	v_permlane32_swap_b32_e32 v16, v18
	v_permlane32_swap_b32_e32 v17, v19
	global_store_dwordx4 v[52:53], v[16:19], off offset:64
	v_pk_mul_f32 v[24:25], v[24:25], v[48:49] op_sel_hi:[1,0]
	v_pk_mul_f32 v[26:27], v[26:27], v[48:49] op_sel_hi:[1,0]
	v_pk_mul_f32 v[28:29], v[28:29], v[48:49] op_sel_hi:[1,0]
	v_pk_mul_f32 v[30:31], v[30:31], v[48:49] op_sel_hi:[1,0]
	v_cvt_pk_bf16_f32 v24, v24, v25
	v_cvt_pk_bf16_f32 v25, v26, v27
	v_cvt_pk_bf16_f32 v26, v28, v29
	v_cvt_pk_bf16_f32 v27, v30, v31
	v_permlane32_swap_b32_e32 v40, v42
	v_permlane32_swap_b32_e32 v41, v43
	global_store_dwordx4 v[52:53], v[40:43], off offset:32
	s_mov_b64 s[14:15], 0
	s_nop 1
	v_permlane32_swap_b32_e32 v24, v26
	v_permlane32_swap_b32_e32 v25, v27
	global_store_dwordx4 v[52:53], v[24:27], off offset:96

.Lpop_nopf:
	s_sub_i32 s16, s26, 2
	s_cmp_lg_u32 s30, s16
	s_cbranch_scc1 .Lwarm_done
	v_readfirstlane_b32 s38, v241
	s_and_b64 s[16:17], exec, s[0:1]
	s_cbranch_scc0 .Lwarm_done
	s_cmp_gt_u32 s38, 0x1ff
	s_cbranch_scc1 .Lwarm_done
	s_and_b32 s40, s38, 31
	s_lshr_b32 s43, s38, 5
	s_sub_i32 s43, 15, s43
	v_mbcnt_lo_u32_b32 v245, -1, 0
	v_mbcnt_hi_u32_b32 v245, -1, v245
	s_mul_i32 s44, s40, 0xc0000
	s_add_u32 s60, s20, s44
	s_addc_u32 s61, s21, 0
	v_lshlrev_b32_e32 v246, 7, v245
	global_load_dword v244, v246, s[60:61]
	s_add_u32 s60, s60, 0x2000
	s_addc_u32 s61, s61, 0
	global_load_dword v244, v246, s[60:61]
	s_add_u32 s60, s60, 0x2000
	s_addc_u32 s61, s61, 0
	global_load_dword v244, v246, s[60:61]
	s_add_u32 s60, s60, 0x2000
	s_addc_u32 s61, s61, 0
	global_load_dword v244, v246, s[60:61]
	s_add_u32 s60, s60, 0x2000
	s_addc_u32 s61, s61, 0
	global_load_dword v244, v246, s[60:61]
	s_lshl_b32 s44, s40, 19
	s_add_u32 s60, s8, 0x2c400000
	s_addc_u32 s61, s9, 0
	s_add_u32 s60, s60, s44
	s_addc_u32 s61, s61, 0
	v_lshlrev_b32_e32 v246, 13, v245
	global_load_dword v244, v246, s[60:61]
	global_load_dword v244, v246, s[60:61] offset:128
	global_load_dword v244, v246, s[60:61] offset:256
	s_lshl_b32 s44, s43, 8
	s_add_i32 s44, s44, s22
	s_lshl_b32 s58, s40, 9
	s_and_b32 s58, s58, 0x3000
	s_add_i32 s44, s44, s58
	s_mul_i32 s44, s44, 0x600
	s_and_b32 s58, s40, 7
	s_mul_i32 s58, s58, 0xc0
	s_add_i32 s44, s44, s58
	s_add_u32 s60, s12, s44
	s_addc_u32 s61, s13, 0
	v_mul_u32_u24_e32 v246, 0x600, v245
	global_load_dword v244, v246, s[60:61]
	global_load_dword v244, v246, s[60:61] offset:128
	s_add_u32 s60, s60, 0x18000
	s_addc_u32 s61, s61, 0
	global_load_dword v244, v246, s[60:61]
	global_load_dword v244, v246, s[60:61] offset:128
	s_add_u32 s60, s60, 0x18000
	s_addc_u32 s61, s61, 0
	global_load_dword v244, v246, s[60:61]
	global_load_dword v244, v246, s[60:61] offset:128
	s_add_u32 s60, s60, 0x18000
	s_addc_u32 s61, s61, 0
	global_load_dword v244, v246, s[60:61]
	global_load_dword v244, v246, s[60:61] offset:128
